# P7 score block: all 8 query-fragment loads of a side issued up front (one round trip instead of four); on top of the P0a colmax rewrite
# speedup vs baseline: 1.1832x; 1.0050x over previous
; #define GAS __attribute__((address_space(1)))
; #define LAS __attribute__((address_space(3)))
; #define MFMA32(a, b, c) __builtin_amdgcn_mfma_f32_32x32x16_bf16((a), (b), (c), 0, 0, 0)
; DI void trow_load(Frame& F, int row, f32x4 (&v)[8]) {
;     if (row < 2 * NEXP) { const int tb = row >= NEXP, e = row - tb * NEXP; const GAS f32x4* src = (const GAS f32x4*)((tb ? F.e_up : F.e_down) + (size_t)e * D) + F.lane;
; #pragma unroll
;         for (int j = 0; j < 8; ++j) v[j] = __builtin_nontemporal_load(src + 64 * j); }
;     else {
; #pragma unroll
;         for (int j = 0; j < 8; ++j) v[j] = (f32x4){0.f, 0.f, 0.f, 0.f}; }
; }
; DI void p8_phase(Frame& F) {
;     ...
;             const bf16* qp = F.QB + (size_t)t * D + hd * 256 + side * 128 + 8 * h;
; #pragma unroll
;             for (int ks = 0; ks < 8; ++ks) {
;                 const bf16x8 qf = __builtin_nontemporal_load((const GAS bf16x8*)(qp + ks * 16));
; #pragma unroll
;                 for (int kt = 0; kt < 4; ++kt) { const bf16x8 kf = *(const LAS bf16x8*)(KIMG + (side * 128 + kt * 32 + r) * KPITCH + (ks * 16 + 8 * h) * 2); acc[kt] = MFMA32(kf, qf, acc[kt]); }
;             }
;             trow_load(F, q0 * NGWT + gcT, ra); trow_load(F, (q0 + 1) * NGWT + gcT, rb);
.LBB0_1208:
	s_lshl_b32 s10, s22, 8
	v_lshl_add_u64 v[94:95], v[142:143], 0, s[10:11]
	global_load_dwordx4 v[66:69], v[94:95], off nt
	global_load_dwordx4 v[70:73], v[94:95], off offset:32 nt
	global_load_dwordx4 v[74:77], v[94:95], off offset:64 nt
	global_load_dwordx4 v[78:81], v[94:95], off offset:96 nt
	global_load_dwordx4 v[82:85], v[94:95], off offset:128 nt
	global_load_dwordx4 v[86:89], v[94:95], off offset:160 nt
	global_load_dwordx4 v[90:93], v[94:95], off offset:192 nt
	global_load_dwordx4 v[100:103], v[94:95], off offset:224 nt
	v_lshl_or_b32 v6, s22, 7, v149
	v_mad_u32_u24 v98, v6, s40, v144
	s_lshl_b32 s10, s22, 2
	s_or_b32 s10, s10, s49
	s_mul_i32 s10, s10, s34
	s_add_i32 s10, s10, s36
	v_lshlrev_b32_e32 v132, 4, v148
	ds_read_b128 v[104:107], v98
	ds_read_b128 v[108:111], v98 offset:8704
	ds_read_b128 v[112:115], v98 offset:17408
	ds_read_b128 v[116:119], v98 offset:26112
	s_waitcnt vmcnt(7) lgkmcnt(3)
	v_mfma_f32_32x32x16_bf16 v[50:65], v[104:107], v[66:69], 0
	s_waitcnt lgkmcnt(2)
	v_mfma_f32_32x32x16_bf16 v[34:49], v[108:111], v[66:69], 0
	s_waitcnt lgkmcnt(1)
	v_mfma_f32_32x32x16_bf16 v[18:33], v[112:115], v[66:69], 0
	s_waitcnt lgkmcnt(0)
	v_mfma_f32_32x32x16_bf16 v[2:17], v[116:119], v[66:69], 0
	ds_read_b128 v[104:107], v98 offset:32
	ds_read_b128 v[108:111], v98 offset:8736
	ds_read_b128 v[112:115], v98 offset:17440
	ds_read_b128 v[116:119], v98 offset:26144
	s_waitcnt vmcnt(6) lgkmcnt(3)
	v_mfma_f32_32x32x16_bf16 v[50:65], v[104:107], v[70:73], v[50:65]
	s_waitcnt lgkmcnt(2)
	v_mfma_f32_32x32x16_bf16 v[34:49], v[108:111], v[70:73], v[34:49]
	s_waitcnt lgkmcnt(1)
	v_mfma_f32_32x32x16_bf16 v[18:33], v[112:115], v[70:73], v[18:33]
	s_waitcnt lgkmcnt(0)
	v_mfma_f32_32x32x16_bf16 v[2:17], v[116:119], v[70:73], v[2:17]
	ds_read_b128 v[104:107], v98 offset:64
	ds_read_b128 v[108:111], v98 offset:8768
	ds_read_b128 v[112:115], v98 offset:17472
	ds_read_b128 v[116:119], v98 offset:26176
	s_waitcnt vmcnt(5) lgkmcnt(3)
	v_mfma_f32_32x32x16_bf16 v[50:65], v[104:107], v[74:77], v[50:65]
	s_waitcnt lgkmcnt(2)
	v_mfma_f32_32x32x16_bf16 v[34:49], v[108:111], v[74:77], v[34:49]
	s_waitcnt lgkmcnt(1)
	v_mfma_f32_32x32x16_bf16 v[18:33], v[112:115], v[74:77], v[18:33]
	s_waitcnt lgkmcnt(0)
	v_mfma_f32_32x32x16_bf16 v[2:17], v[116:119], v[74:77], v[2:17]
	ds_read_b128 v[104:107], v98 offset:96
	ds_read_b128 v[108:111], v98 offset:8800
	ds_read_b128 v[112:115], v98 offset:17504
	ds_read_b128 v[116:119], v98 offset:26208
	s_waitcnt vmcnt(4) lgkmcnt(3)
	v_mfma_f32_32x32x16_bf16 v[50:65], v[104:107], v[78:81], v[50:65]
	s_waitcnt lgkmcnt(2)
	v_mfma_f32_32x32x16_bf16 v[34:49], v[108:111], v[78:81], v[34:49]
	s_waitcnt lgkmcnt(1)
	v_mfma_f32_32x32x16_bf16 v[18:33], v[112:115], v[78:81], v[18:33]
	s_waitcnt lgkmcnt(0)
	v_mfma_f32_32x32x16_bf16 v[2:17], v[116:119], v[78:81], v[2:17]
	ds_read_b128 v[104:107], v98 offset:128
	ds_read_b128 v[108:111], v98 offset:8832
	ds_read_b128 v[112:115], v98 offset:17536
	ds_read_b128 v[116:119], v98 offset:26240
	s_waitcnt vmcnt(3) lgkmcnt(3)
	v_mfma_f32_32x32x16_bf16 v[50:65], v[104:107], v[82:85], v[50:65]
	s_waitcnt lgkmcnt(2)
	v_mfma_f32_32x32x16_bf16 v[34:49], v[108:111], v[82:85], v[34:49]
	s_waitcnt lgkmcnt(1)
	v_mfma_f32_32x32x16_bf16 v[18:33], v[112:115], v[82:85], v[18:33]
	s_waitcnt lgkmcnt(0)
	v_mfma_f32_32x32x16_bf16 v[2:17], v[116:119], v[82:85], v[2:17]
	ds_read_b128 v[104:107], v98 offset:160
	ds_read_b128 v[108:111], v98 offset:8864
	ds_read_b128 v[112:115], v98 offset:17568
	ds_read_b128 v[116:119], v98 offset:26272
	s_waitcnt vmcnt(2) lgkmcnt(3)
	v_mfma_f32_32x32x16_bf16 v[50:65], v[104:107], v[86:89], v[50:65]
	s_waitcnt lgkmcnt(2)
	v_mfma_f32_32x32x16_bf16 v[34:49], v[108:111], v[86:89], v[34:49]
	s_waitcnt lgkmcnt(1)
	v_mfma_f32_32x32x16_bf16 v[18:33], v[112:115], v[86:89], v[18:33]
	s_waitcnt lgkmcnt(0)
	v_mfma_f32_32x32x16_bf16 v[2:17], v[116:119], v[86:89], v[2:17]
	ds_read_b128 v[104:107], v98 offset:192
	ds_read_b128 v[108:111], v98 offset:8896
	ds_read_b128 v[112:115], v98 offset:17600
	ds_read_b128 v[116:119], v98 offset:26304
	s_waitcnt vmcnt(1) lgkmcnt(3)
	v_mfma_f32_32x32x16_bf16 v[50:65], v[104:107], v[90:93], v[50:65]
	s_waitcnt lgkmcnt(2)
	v_mfma_f32_32x32x16_bf16 v[34:49], v[108:111], v[90:93], v[34:49]
	s_waitcnt lgkmcnt(1)
	v_mfma_f32_32x32x16_bf16 v[18:33], v[112:115], v[90:93], v[18:33]
	s_waitcnt lgkmcnt(0)
	v_mfma_f32_32x32x16_bf16 v[2:17], v[116:119], v[90:93], v[2:17]
	ds_read_b128 v[104:107], v98 offset:224
	ds_read_b128 v[108:111], v98 offset:8928
	ds_read_b128 v[112:115], v98 offset:17632
	ds_read_b128 v[116:119], v98 offset:26336
	s_waitcnt vmcnt(0) lgkmcnt(3)
	v_mfma_f32_32x32x16_bf16 v[50:65], v[104:107], v[100:103], v[50:65]
	s_waitcnt lgkmcnt(2)
	v_mfma_f32_32x32x16_bf16 v[34:49], v[108:111], v[100:103], v[34:49]
	s_waitcnt lgkmcnt(1)
	v_mfma_f32_32x32x16_bf16 v[18:33], v[112:115], v[100:103], v[18:33]
	s_waitcnt lgkmcnt(0)
	v_mfma_f32_32x32x16_bf16 v[2:17], v[116:119], v[100:103], v[2:17]
	v_mov_b32_e32 v126, 0
	v_mov_b32_e32 v127, 0
	v_mov_b32_e32 v128, 0
	v_mov_b32_e32 v129, 0
	v_mov_b32_e32 v122, 0
	v_mov_b32_e32 v123, 0
	v_mov_b32_e32 v124, 0
	v_mov_b32_e32 v125, 0
	v_mov_b32_e32 v114, 0
	v_mov_b32_e32 v115, 0
	v_mov_b32_e32 v116, 0
	v_mov_b32_e32 v117, 0
	v_mov_b32_e32 v106, 0
	v_mov_b32_e32 v107, 0
	v_mov_b32_e32 v108, 0
	v_mov_b32_e32 v109, 0
	v_mov_b32_e32 v98, 0
	v_mov_b32_e32 v99, 0
	v_mov_b32_e32 v100, 0
	v_mov_b32_e32 v101, 0
	v_mov_b32_e32 v90, 0
	v_mov_b32_e32 v91, 0
	v_mov_b32_e32 v92, 0
	v_mov_b32_e32 v93, 0
	v_mov_b32_e32 v78, 0
	v_mov_b32_e32 v79, 0
	v_mov_b32_e32 v80, 0
	v_mov_b32_e32 v81, 0
	v_mov_b32_e32 v86, 0
	v_mov_b32_e32 v87, 0
	v_mov_b32_e32 v88, 0
	v_mov_b32_e32 v89, 0
	v_mov_b32_e32 v66, 0
	s_cmpk_gt_i32 s10, 0x7fff
	s_cbranch_scc1 .LBB0_1210
	s_cmpk_gt_i32 s10, 0x3fff
	s_cselect_b32 s12, 0xffffc000, 0
	s_cselect_b32 s22, s82, s80
	s_cselect_b32 s23, s83, s81
	s_add_i32 s12, s12, s10
	s_ashr_i32 s13, s12, 31
	s_lshl_b64 s[12:13], s[12:13], 13
	s_add_u32 s12, s22, s12
	s_addc_u32 s13, s23, s13
	v_lshl_add_u64 v[68:69], s[12:13], 0, v[132:133]
	v_add_co_u32_e32 v68, vcc, s41, v68
	global_load_dwordx4 v[126:129], v132, s[12:13] nt
	global_load_dwordx4 v[122:125], v132, s[12:13] offset:1024 nt
	global_load_dwordx4 v[114:117], v132, s[12:13] offset:2048 nt
	global_load_dwordx4 v[106:109], v132, s[12:13] offset:3072 nt
	v_addc_co_u32_e32 v69, vcc, 0, v69, vcc
	global_load_dwordx4 v[98:101], v[68:69], off nt
	global_load_dwordx4 v[90:93], v[68:69], off offset:1024 nt
	global_load_dwordx4 v[78:81], v[68:69], off offset:2048 nt
	global_load_dwordx4 v[86:89], v[68:69], off offset:3072 nt
